# attention K/V LDS tile pitch 144 B -> 160 B (removes 2-way bank conflicts on ds_read_b128 K and ds_read_b64_tr_b16 V reads) on top of chain DMA reorder
# speedup vs baseline: 1.0046x; 1.0046x over previous
; #define GAS __attribute__((address_space(1)))
; #define LAS __attribute__((address_space(3)))
; DI int rfl(int v) { return __builtin_amdgcn_readfirstlane(v); }
; DI int ltid() { int t = threadIdx.x; asm volatile("" : "+v"(t)); return t; }
; #define AT_BAR() do { asm volatile("s_waitcnt lgkmcnt(0)" ::: "memory"); __builtin_amdgcn_s_barrier(); asm volatile("" ::: "memory"); } while (0)
; DI void attn_load(const Ctx& c, int u, APre& p) {
;     const int tid = ltid(), lane = tid & 63, w = rfl(tid >> 6), fr = lane & 15, fq = lane >> 4; const AUnit a = attn_decode(u);
;     const GAS char* Q = (const GAS char*)(c.ws + WS_H + H_QD) + a.slab; const GAS char* K = (const GAS char*)(c.ws + WS_H + H_KD) + a.slab; const GAS char* V = (const GAS char*)(c.ws + WS_H + H_VD) + a.slab;
; #pragma unroll
;     for (int b = 0; b < 2; ++b) { const unsigned jq = (unsigned)(128 * (a.n + b) + 16 * w + fr);
; #pragma unroll
;         for (int d0 = 0; d0 < 2; ++d0) p.q[b][d0] = *(const GAS u32x2*)(Q + (jq * 64u + (unsigned)(32 * d0 + 8 * fq))); }
; #pragma unroll
;     for (int c2 = 0; c2 < 6; ++c2) { const int idx = tid + NTHREADS * c2, row = idx >> 3, ch = idx & 7; const int j = 128 * (a.n - 1) + row;
;         p.k[c2] = (u32x2){0u, 0u}; p.v[c2] = (u32x2){0u, 0u};
;         if (j >= 0) { const unsigned off = (unsigned)j * 64u + (unsigned)(ch * 8); p.k[c2] = *(const GAS u32x2*)(K + off); p.v[c2] = *(const GAS u32x2*)(V + off); } }
; }
; DI void attn_stage(LAS unsigned char* lds, const APre& p) {
;     const int tid = ltid(); LAS bf16_t* Ks = (LAS bf16_t*)(lds + AT_K); LAS bf16_t* Vs = (LAS bf16_t*)(lds + AT_V);
; #pragma unroll
;     for (int c2 = 0; c2 < 6; ++c2) { const int o = (tid >> 3) * 72 + (tid & 7) * 8 + c2 * (64 * 72); *(LAS u32x4*)(Ks + o) = fp8x8_to_bf16(p.k[c2]); *(LAS u32x4*)(Vs + o) = fp8x8_to_bf16(p.v[c2]); }
; }
; DI void attn_pull(LAS unsigned char* lds, const Ctx& c, unsigned* ctr, int base, int limit) {
;     ...
;     while (cur < limit) {
;         AT_BAR();
;         const int nxt2 = rfl(TK[2]);
;         attn_stage(lds, pre);
;         bf16x8 qf[2][2];
; #pragma unroll
;         for (int b = 0; b < 2; ++b)
; #pragma unroll
;             for (int d0 = 0; d0 < 2; ++d0) qf[b][d0] = __builtin_bit_cast(bf16x8, fp8x8_to_bf16(pre.q[b][d0]));
;         AT_BAR();
;         if (nxt < limit) attn_load(c, nxt, pre);
.LBB0_675:
	s_waitcnt lgkmcnt(0)
	s_barrier
	v_mov_b32_e32 v1, s78
	v_mov_b32_e32 v5, v0
	ds_read_b32 v1, v1
	s_movk_i32 s7, 0x50
	v_lshrrev_b32_e32 v9, 3, v5
	v_lshlrev_b32_e32 v5, 3, v5
	v_and_b32_e32 v8, 56, v5
	v_mad_u64_u32 v[12:13], s[8:9], v9, s7, v[8:9]
	v_cvt_pk_f32_fp8_e32 v[8:9], v44
	v_cvt_pk_f32_fp8_sdwa v[10:11], v44 src0_sel:WORD_1
	v_cvt_pk_f32_fp8_e32 v[14:15], v45
	v_cvt_pk_f32_fp8_sdwa v[16:17], v45 src0_sel:WORD_1
	v_cvt_pk_bf16_f32 v8, v8, v9
	v_cvt_pk_bf16_f32 v9, v10, v11
	v_cvt_pk_bf16_f32 v10, v14, v15
	v_cvt_pk_bf16_f32 v11, v16, v17
	v_lshl_add_u32 v5, v12, 1, s38
	v_add_u32_e32 v196, 0xf000, v5
	ds_write_b128 v5, v[8:11]
	v_cvt_pk_f32_fp8_e32 v[8:9], v46
	v_cvt_pk_f32_fp8_sdwa v[10:11], v46 src0_sel:WORD_1
	v_cvt_pk_f32_fp8_e32 v[12:13], v47
	v_cvt_pk_f32_fp8_sdwa v[14:15], v47 src0_sel:WORD_1
	v_cvt_pk_bf16_f32 v8, v8, v9
	v_cvt_pk_bf16_f32 v9, v10, v11
	v_cvt_pk_bf16_f32 v10, v12, v13
	v_cvt_pk_bf16_f32 v11, v14, v15
	ds_write_b128 v196, v[8:11]
	v_cvt_pk_f32_fp8_e32 v[8:9], v48
	v_cvt_pk_f32_fp8_sdwa v[10:11], v48 src0_sel:WORD_1
	v_cvt_pk_f32_fp8_e32 v[12:13], v49
	v_cvt_pk_f32_fp8_sdwa v[14:15], v49 src0_sel:WORD_1
	v_cvt_pk_bf16_f32 v8, v8, v9
	v_cvt_pk_bf16_f32 v9, v10, v11
	v_cvt_pk_bf16_f32 v10, v12, v13
	v_cvt_pk_bf16_f32 v11, v14, v15
	ds_write_b128 v5, v[8:11] offset:10240
	v_cvt_pk_f32_fp8_e32 v[8:9], v42
	v_cvt_pk_f32_fp8_sdwa v[10:11], v42 src0_sel:WORD_1
	v_cvt_pk_f32_fp8_e32 v[12:13], v43
	v_cvt_pk_f32_fp8_sdwa v[14:15], v43 src0_sel:WORD_1
	v_cvt_pk_bf16_f32 v8, v8, v9
	v_cvt_pk_bf16_f32 v9, v10, v11
	v_cvt_pk_bf16_f32 v10, v12, v13
	v_cvt_pk_bf16_f32 v11, v14, v15
	ds_write_b128 v196, v[8:11] offset:10240
	v_cvt_pk_f32_fp8_e32 v[8:9], v50
	v_cvt_pk_f32_fp8_sdwa v[10:11], v50 src0_sel:WORD_1
	v_cvt_pk_f32_fp8_e32 v[12:13], v51
	v_cvt_pk_f32_fp8_sdwa v[14:15], v51 src0_sel:WORD_1
	v_cvt_pk_bf16_f32 v8, v8, v9
	v_cvt_pk_bf16_f32 v9, v10, v11
	v_cvt_pk_bf16_f32 v10, v12, v13
	v_cvt_pk_bf16_f32 v11, v14, v15
	ds_write_b128 v5, v[8:11] offset:20480
	v_cvt_pk_f32_fp8_e32 v[8:9], v52
	v_cvt_pk_f32_fp8_sdwa v[10:11], v52 src0_sel:WORD_1
	v_cvt_pk_f32_fp8_e32 v[12:13], v53
	v_cvt_pk_f32_fp8_sdwa v[14:15], v53 src0_sel:WORD_1
	v_add_u32_e32 v16, 0xd800, v5
	v_cvt_pk_bf16_f32 v8, v8, v9
	v_cvt_pk_bf16_f32 v9, v10, v11
	v_cvt_pk_bf16_f32 v10, v12, v13
	v_cvt_pk_bf16_f32 v11, v14, v15
	ds_write_b128 v196, v[8:11] offset:20480
	v_cvt_pk_f32_fp8_e32 v[8:9], v62
	v_cvt_pk_f32_fp8_sdwa v[10:11], v62 src0_sel:WORD_1
	v_cvt_pk_f32_fp8_e32 v[12:13], v63
	v_cvt_pk_f32_fp8_sdwa v[14:15], v63 src0_sel:WORD_1
	v_cvt_pk_bf16_f32 v8, v8, v9
	v_cvt_pk_bf16_f32 v9, v10, v11
	v_cvt_pk_bf16_f32 v10, v12, v13
	v_cvt_pk_bf16_f32 v11, v14, v15
	ds_write_b128 v5, v[8:11] offset:30720
	v_cvt_pk_f32_fp8_e32 v[8:9], v64
	v_cvt_pk_f32_fp8_sdwa v[10:11], v64 src0_sel:WORD_1
	v_cvt_pk_f32_fp8_e32 v[12:13], v65
	v_cvt_pk_f32_fp8_sdwa v[14:15], v65 src0_sel:WORD_1
	v_cvt_pk_bf16_f32 v8, v8, v9
	v_cvt_pk_bf16_f32 v9, v10, v11
	v_cvt_pk_bf16_f32 v10, v12, v13
	v_cvt_pk_bf16_f32 v11, v14, v15
	ds_write_b128 v196, v[8:11] offset:30720
	v_cvt_pk_f32_fp8_e32 v[8:9], v66
	v_cvt_pk_f32_fp8_sdwa v[10:11], v66 src0_sel:WORD_1
	v_cvt_pk_f32_fp8_e32 v[12:13], v67
	v_cvt_pk_f32_fp8_sdwa v[14:15], v67 src0_sel:WORD_1
	v_cvt_pk_bf16_f32 v8, v8, v9
	v_cvt_pk_bf16_f32 v9, v10, v11
	v_cvt_pk_bf16_f32 v10, v12, v13
	v_cvt_pk_bf16_f32 v11, v14, v15
	ds_write_b128 v5, v[8:11] offset:40960
	v_cvt_pk_f32_fp8_e32 v[8:9], v68
	v_cvt_pk_f32_fp8_sdwa v[10:11], v68 src0_sel:WORD_1
	v_cvt_pk_f32_fp8_e32 v[12:13], v69
	v_cvt_pk_f32_fp8_sdwa v[14:15], v69 src0_sel:WORD_1
	v_cvt_pk_bf16_f32 v8, v8, v9
	v_cvt_pk_bf16_f32 v9, v10, v11
	v_cvt_pk_bf16_f32 v10, v12, v13
	v_cvt_pk_bf16_f32 v11, v14, v15
	ds_write_b128 v196, v[8:11] offset:40960
	v_cvt_pk_f32_fp8_e32 v[8:9], v70
	v_cvt_pk_f32_fp8_sdwa v[10:11], v70 src0_sel:WORD_1
	v_cvt_pk_f32_fp8_e32 v[12:13], v71
	v_cvt_pk_f32_fp8_sdwa v[14:15], v71 src0_sel:WORD_1
	v_cvt_pk_bf16_f32 v8, v8, v9
	v_cvt_pk_bf16_f32 v9, v10, v11
	v_cvt_pk_bf16_f32 v10, v12, v13
	v_cvt_pk_bf16_f32 v11, v14, v15
	ds_write_b128 v5, v[8:11] offset:51200
	v_cvt_pk_f32_fp8_e32 v[8:9], v72
	v_cvt_pk_f32_fp8_sdwa v[10:11], v72 src0_sel:WORD_1
	v_cvt_pk_f32_fp8_e32 v[12:13], v73
	v_cvt_pk_f32_fp8_sdwa v[14:15], v73 src0_sel:WORD_1
	v_cvt_pk_bf16_f32 v8, v8, v9
	v_cvt_pk_bf16_f32 v9, v10, v11
	v_cvt_pk_bf16_f32 v10, v12, v13
	v_cvt_pk_bf16_f32 v11, v14, v15
	ds_write_b128 v196, v[8:11] offset:51200
	s_waitcnt lgkmcnt(0)
	s_barrier
	s_cmpk_gt_i32 s4, 0x5ff
	s_cselect_b64 s[62:63], -1, 0
	s_waitcnt lgkmcnt(12)
	v_readfirstlane_b32 s79, v1
	s_and_b64 vcc, exec, s[62:63]
	s_cbranch_vccnz .LBB0_689
	s_ashr_i32 s8, s4, 31
	s_lshr_b32 s8, s8, 24
	s_add_i32 s8, s4, s8
	s_ashr_i32 s8, s8, 8
	s_mul_hi_i32 s9, s8, 0x55555556
	s_lshr_b32 s10, s9, 31
	s_add_i32 s9, s9, s10
	s_mul_hi_i32 s10, s4, 0x2aaaaaab
	s_mul_i32 s9, s9, 3
	s_lshr_b32 s11, s10, 31
	s_lshr_b32 s10, s10, 7
	s_sub_i32 s8, s8, s9
	s_and_b32 s9, s4, 31
	s_add_i32 s10, s10, s11
	s_cmp_eq_u32 s8, 1
	s_cselect_b32 s11, 2, 4
	s_cmp_lg_u32 s8, 0
	s_cselect_b32 s11, s11, 0
	s_sub_i32 s43, 5, s11
	s_lshr_b32 s42, 32, s11
	s_lshr_b32 s43, s9, s43
	s_mul_i32 s42, s43, s42
	s_sub_i32 s46, s9, s42
	s_sub_i32 s9, 12, s11
	s_lshl_b32 s11, s4, 16
	s_and_b32 s11, s11, 0xe00000
	s_lshl_b32 s10, s10, 18
	s_lshl_b32 s9, s43, s9
	s_lshl_b32 s8, s8, 24
	s_add_i32 s10, s11, s10
	s_add_i32 s8, s10, s8
	s_lshl_b32 s9, s9, 6
	v_mov_b32_e32 v1, v0
	s_add_i32 s10, s8, s9
	s_add_u32 s8, s5, s10
	v_readfirstlane_b32 s7, v1
	s_addc_u32 s9, s39, 0
	s_lshr_b32 s7, s7, 2
	s_and_b32 s7, s7, 0x3fffff0
	v_and_or_b32 v5, v1, 15, s7
	s_lshl_b32 s7, s46, 13
	v_lshrrev_b32_e32 v8, 1, v1
	v_lshl_add_u32 v5, v5, 6, s7
	v_and_or_b32 v5, v8, 24, v5
	v_add_u32_e32 v8, 0x2000, v5
	global_load_dwordx2 v[60:61], v5, s[8:9]
	global_load_dwordx2 v[58:59], v5, s[8:9] offset:32
	global_load_dwordx2 v[56:57], v8, s[8:9]
	global_load_dwordx2 v[54:55], v8, s[8:9] offset:32
	s_add_u32 s42, s68, s10
	s_addc_u32 s43, s74, 0
	s_add_u32 s44, s75, s10
	s_addc_u32 s45, s76, 0
	s_lshl_b32 s7, s46, 7
	v_lshlrev_b32_e32 v5, 3, v1
	s_addk_i32 s7, 0xff80
	v_and_b32_e32 v8, 56, v5
	v_ashrrev_i32_e32 v5, 3, v1
	v_add_u32_e32 v5, s7, v5
	v_mov_b32_e32 v42, v4
	v_mov_b32_e32 v43, v4
	v_cmp_lt_i32_e32 vcc, -1, v5
	v_mov_b64_e32 v[46:47], v[42:43]
	v_mov_b64_e32 v[44:45], v[42:43]
	s_and_saveexec_b64 s[46:47], vcc
	s_cbranch_execz .LBB0_678
	v_lshl_or_b32 v5, v5, 6, v8
	global_load_dwordx2 v[44:45], v5, s[42:43]
	global_load_dwordx2 v[46:47], v5, s[44:45]

; #define LAS __attribute__((address_space(3)))
; DI int rfl(int v) { return __builtin_amdgcn_readfirstlane(v); }
; DI int ltid() { int t = threadIdx.x; asm volatile("" : "+v"(t)); return t; }
; #define MFMA16(a, b, c) __builtin_amdgcn_mfma_f32_16x16x32_bf16((a), (b), (c), 0, 0, 0)
; DI void attn_compute(LAS unsigned char* lds, const Ctx& c, int u, const bf16x8 (&qf)[2][2]) {
;     const int tid = ltid(), lane = tid & 63, w = rfl(tid >> 6), fr = lane & 15, fq = lane >> 4; const AUnit au = attn_decode(u);
;     const int dl = au.dl, n = au.n, g = (u / 256) % 3, h = (u >> 5) & 7; const unsigned tb = au.tb;
;     LAS bf16_t* Ks = (LAS bf16_t*)(lds + AT_K); LAS bf16_t* Vs = (LAS bf16_t*)(lds + AT_V);
; #pragma unroll
;     for (int b = 0; b < 2; ++b) {
;         const int kt0 = 8 * b + w;
;         const LAS bf16_t* kbase = Ks + (16 * w + fr) * 72 + 8 * fq + b * (128 * 72);
;         const LAS bf16_t* vbase = Vs + (16 * w + 4 * fq + (fr >> 2)) * 72 + (fr & 3) * 4 + b * (128 * 72);
;         f32x4 s[9]; float m = -1e30f;
; #pragma unroll
;         for (int kr = 0; kr < 9; ++kr) { const int kt = kt0 + kr; f32x4 a = (f32x4){0.f, 0.f, 0.f, 0.f};
; #pragma unroll
;             for (int d0 = 0; d0 < 2; ++d0) { const bf16x8 af = *(const LAS bf16x8*)(kbase + kr * (16 * 72) + 32 * d0); a = MFMA16(af, qf[b][d0], a); }
; #pragma unroll
;             for (int rg = 0; rg < 4; ++rg) { const bool tile_ok = (b > 0) || (n > 0) || (kt >= 8);
;                 bool ok = tile_ok; if (kr == 0) ok = ok && (4 * fq + rg >= fr); if (kr == 8) ok = ok && (4 * fq + rg <= fr);
;                 a[rg] = ok ? a[rg] : -1e30f; m = fmaxf(m, a[rg]); }
;             s[kr] = a; }
.LBB0_693:
	s_or_b64 exec, exec, s[42:43]
	v_cvt_pk_f32_fp8_e32 v[8:9], v6
	v_cvt_pk_f32_fp8_sdwa v[10:11], v6 src0_sel:WORD_1
	v_cvt_pk_f32_fp8_e32 v[12:13], v7
	v_cvt_pk_f32_fp8_sdwa v[6:7], v7 src0_sel:WORD_1
	s_ashr_i32 s8, s6, 31
	s_lshr_b32 s8, s8, 24
	s_add_i32 s8, s6, s8
	s_ashr_i32 s8, s8, 8
	v_cvt_pk_bf16_f32 v14, v8, v9
	v_cvt_pk_bf16_f32 v15, v10, v11
	v_cvt_pk_bf16_f32 v17, v6, v7
	v_cvt_pk_f32_fp8_e32 v[6:7], v2
	v_cvt_pk_f32_fp8_sdwa v[8:9], v2 src0_sel:WORD_1
	v_cvt_pk_f32_fp8_e32 v[10:11], v3
	v_cvt_pk_f32_fp8_sdwa v[2:3], v3 src0_sel:WORD_1
	s_mul_hi_i32 s9, s8, 0x55555556
	s_lshr_b32 s10, s9, 31
	s_add_i32 s9, s9, s10
	s_mul_i32 s9, s9, 3
	v_cvt_pk_bf16_f32 v21, v2, v3
	v_mov_b32_e32 v2, v0
	s_sub_i32 s9, s8, s9
	s_and_b32 s8, s6, 31
	s_bfe_u32 s10, s6, 0x30005
	s_mul_hi_i32 s6, s6, 0x2aaaaaab
	s_lshr_b32 s11, s6, 31
	v_readfirstlane_b32 s7, v2
	s_lshr_b32 s6, s6, 7
	s_ashr_i32 s7, s7, 6
	s_add_i32 s11, s6, s11
	s_cmp_eq_u32 s9, 1
	s_cselect_b32 s6, 2, 4
	s_cmp_lg_u32 s9, 0
	s_cselect_b32 s81, s6, 0
	s_sub_i32 s42, 5, s81
	s_lshr_b32 s6, 32, s81
	s_lshr_b32 s44, s8, s42
	s_mul_i32 s6, s44, s6
	v_and_b32_e32 v3, 15, v2
	s_sub_i32 s6, s8, s6
	s_lshl_b32 s8, s7, 4
	v_or_b32_e32 v27, s8, v3
	v_bfe_u32 v26, v2, 4, 2
	s_movk_i32 s100, 0xa0
	v_mul_lo_u32 v5, v27, s100
	v_cvt_pk_bf16_f32 v18, v6, v7
	v_add_u32_e32 v5, s38, v5
	v_lshlrev_b32_e32 v6, 4, v26
	v_add_u32_e32 v74, v5, v6
	v_cvt_pk_bf16_f32 v19, v8, v9
	ds_read_b128 v[6:9], v74
	v_cvt_pk_bf16_f32 v20, v10, v11
	v_and_b32_e32 v10, 64, v202
	v_cvt_pk_bf16_f32 v16, v12, v13
	v_add_u32_e32 v32, 64, v10
	ds_read_b128 v[10:13], v74 offset:64
	s_lshl_b32 s11, s11, 12
	s_lshl_b32 s82, s10, 6
	s_cmp_gt_i32 s6, 0
	s_waitcnt lgkmcnt(1)
	v_mfma_f32_16x16x32_bf16 v[6:9], v[6:9], v[14:17], 0
	s_cselect_b64 s[42:43], -1, 0
	s_lshl_b32 s9, s9, 15
	s_add_i32 s9, s9, s11
	s_or_b32 s83, s44, s9
	s_lshl_b32 s80, s10, 2
	s_waitcnt lgkmcnt(0)
	v_mfma_f32_16x16x32_bf16 v[6:9], v[10:13], v[18:21], v[6:9]
	s_cmp_gt_i32 s7, 7
	v_lshlrev_b32_e32 v80, 2, v26
	v_xor_b32_e32 v28, 16, v202
	s_cselect_b64 s[10:11], -1, 0
	ds_read_b128 v[10:13], v74 offset:2560
	v_cmp_lt_i32_e32 vcc, v28, v32
	v_cmp_ge_u32_e64 s[52:53], v80, v3
	s_or_b64 s[10:11], s[42:43], s[10:11]
	v_cndmask_b32_e32 v28, v202, v28, vcc
	s_and_b64 vcc, s[10:11], s[52:53]
	v_cndmask_b32_e32 v33, v209, v6, vcc
	v_or_b32_e32 v6, 1, v80
	v_lshlrev_b32_e32 v83, 2, v28
	v_cmp_ge_u32_e64 s[54:55], v6, v3
	v_or_b32_e32 v35, 2, v80
	ds_read_b128 v[28:31], v74 offset:2624
	s_and_b64 vcc, s[10:11], s[54:55]
	v_cmp_ge_u32_e64 s[56:57], v35, v3
	v_or_b32_e32 v37, 3, v80
	v_cndmask_b32_e32 v34, v209, v7, vcc
	s_and_b64 vcc, s[10:11], s[56:57]
	v_cmp_ge_u32_e64 s[58:59], v37, v3
	s_mov_b32 s9, 0xf149f2ca
	v_cndmask_b32_e32 v36, v209, v8, vcc
	s_and_b64 vcc, s[10:11], s[58:59]
	v_max3_f32 v6, v33, s9, v34
	v_cndmask_b32_e32 v38, v209, v9, vcc
	s_waitcnt lgkmcnt(1)
	v_mfma_f32_16x16x32_bf16 v[10:13], v[10:13], v[14:17], 0
	v_max3_f32 v39, v6, v36, v38
	ds_read_b128 v[6:9], v74 offset:5120
	s_cmp_gt_i32 s7, 6
	s_waitcnt lgkmcnt(1)
	v_mfma_f32_16x16x32_bf16 v[10:13], v[28:31], v[18:21], v[10:13]
	ds_read_b128 v[28:31], v74 offset:5184
	s_cselect_b64 s[10:11], -1, 0
	s_or_b64 vcc, s[42:43], s[10:11]
	s_waitcnt lgkmcnt(1)
	v_mfma_f32_16x16x32_bf16 v[6:9], v[6:9], v[14:17], 0
	s_cmp_gt_i32 s7, 5
	s_nop 1
	v_cndmask_b32_e32 v40, v209, v10, vcc
	v_cndmask_b32_e32 v41, v209, v11, vcc
	v_max3_f32 v10, v39, v40, v41
	v_cndmask_b32_e32 v39, v209, v12, vcc
	v_cndmask_b32_e32 v75, v209, v13, vcc
	v_max3_f32 v76, v10, v39, v75
	ds_read_b128 v[10:13], v74 offset:7680
	s_waitcnt lgkmcnt(1)
	v_mfma_f32_16x16x32_bf16 v[6:9], v[28:31], v[18:21], v[6:9]
	ds_read_b128 v[28:31], v74 offset:7744
	s_cselect_b64 s[10:11], -1, 0
	s_or_b64 vcc, s[42:43], s[10:11]
	s_waitcnt lgkmcnt(1)
	v_mfma_f32_16x16x32_bf16 v[10:13], v[10:13], v[14:17], 0
	s_nop 2
	v_cndmask_b32_e32 v77, v209, v6, vcc
	v_cndmask_b32_e32 v78, v209, v7, vcc
	v_max3_f32 v6, v76, v77, v78
	v_cndmask_b32_e32 v76, v209, v8, vcc
	v_cndmask_b32_e32 v79, v209, v9, vcc
	v_max3_f32 v81, v6, v76, v79
	ds_read_b128 v[6:9], v74 offset:10240
	s_waitcnt lgkmcnt(1)
	v_mfma_f32_16x16x32_bf16 v[10:13], v[28:31], v[18:21], v[10:13]
	ds_read_b128 v[28:31], v74 offset:10304
	s_cmp_gt_i32 s7, 4
	s_cselect_b64 s[10:11], -1, 0
	s_or_b64 vcc, s[42:43], s[10:11]
	s_waitcnt lgkmcnt(1)
	v_mfma_f32_16x16x32_bf16 v[6:9], v[6:9], v[14:17], 0
	s_nop 1
	v_cndmask_b32_e32 v82, v209, v10, vcc
	v_cndmask_b32_e32 v84, v209, v11, vcc
	v_max3_f32 v10, v81, v82, v84
	v_cndmask_b32_e32 v88, v209, v12, vcc
	v_cndmask_b32_e32 v89, v209, v13, vcc
	v_max3_f32 v81, v10, v88, v89
	ds_read_b128 v[10:13], v74 offset:12800
	s_waitcnt lgkmcnt(1)
	v_mfma_f32_16x16x32_bf16 v[6:9], v[28:31], v[18:21], v[6:9]
	s_cmp_gt_i32 s7, 3
	ds_read_b128 v[28:31], v74 offset:12864
	s_cselect_b64 s[10:11], -1, 0
	s_or_b64 vcc, s[42:43], s[10:11]
	s_waitcnt lgkmcnt(1)
	v_mfma_f32_16x16x32_bf16 v[10:13], v[10:13], v[14:17], 0
	s_nop 1
	v_cndmask_b32_e32 v94, v209, v6, vcc
	v_cndmask_b32_e32 v95, v209, v7, vcc
	v_max3_f32 v6, v81, v94, v95
	v_cndmask_b32_e32 v96, v209, v8, vcc
	v_cndmask_b32_e32 v97, v209, v9, vcc
	v_max3_f32 v81, v6, v96, v97
	ds_read_b128 v[6:9], v74 offset:15360
	s_waitcnt lgkmcnt(1)
	v_mfma_f32_16x16x32_bf16 v[10:13], v[28:31], v[18:21], v[10:13]
	ds_read_b128 v[28:31], v74 offset:15424
	s_cmp_gt_i32 s7, 2
	s_cselect_b64 s[10:11], -1, 0
	s_or_b64 vcc, s[42:43], s[10:11]
	s_waitcnt lgkmcnt(1)
; #define LAS __attribute__((address_space(3)))
; DI unsigned cvt_pk_bf16(float lo, float hi) { f32x2 v = {lo, hi}; bf16x2_t b = __builtin_convertvector(v, bf16x2_t); return __builtin_bit_cast(unsigned, b); }
; DI s16x4 tr16(const LAS void* p) { return __builtin_bit_cast(s16x4, __builtin_amdgcn_ds_read_tr16_b64_v4i16((LAS s16x4*)p)); }
; DI bf16x8 cat8(s16x4 lo, s16x4 hi) { return __builtin_shufflevector(lo, hi, 0, 1, 2, 3, 4, 5, 6, 7); }
; DI void attn_compute(LAS unsigned char* lds, const Ctx& c, int u, const bf16x8 (&qf)[2][2]) {
;     ...
;             for (int d0 = 0; d0 < 2; ++d0) { const bf16x8 af = *(const LAS bf16x8*)(kbase + kr * (16 * 72) + 32 * d0); a = MFMA16(af, qf[b][d0], a); }
; #pragma unroll
;             for (int rg = 0; rg < 4; ++rg) { const bool tile_ok = (b > 0) || (n > 0) || (kt >= 8);
;                 bool ok = tile_ok; if (kr == 0) ok = ok && (4 * fq + rg >= fr); if (kr == 8) ok = ok && (4 * fq + rg <= fr);
;                 a[rg] = ok ? a[rg] : -1e30f; m = fmaxf(m, a[rg]); }
;             s[kr] = a; }
;         m = fmaxf(m, __shfl_xor(m, 16)); m = fmaxf(m, __shfl_xor(m, 32));
;         f32x4 ls4 = (f32x4){0.f, 0.f, 0.f, 0.f}; const f32x4 m4 = (f32x4){m, m, m, m};
; #pragma unroll
;         for (int kr = 0; kr < 9; ++kr) { const f32x4 d = s[kr] - m4;
;             s[kr] = (f32x4){__builtin_amdgcn_exp2f(d[0]), __builtin_amdgcn_exp2f(d[1]), __builtin_amdgcn_exp2f(d[2]), __builtin_amdgcn_exp2f(d[3])}; ls4 += s[kr]; }
;         float lsum = (ls4[0] + ls4[1]) + (ls4[2] + ls4[3]);
;         lsum += __shfl_xor(lsum, 16); lsum += __shfl_xor(lsum, 32);
;         f32x4 oT[4];
; #pragma unroll
;         for (int dt = 0; dt < 4; ++dt) oT[dt] = (f32x4){0.f, 0.f, 0.f, 0.f};
; #pragma unroll
;         for (int pp = 0; pp < 5; ++pp) { const int ka = 2 * pp, kb = (2 * pp + 1 < 9) ? 2 * pp + 1 : 8;
;             u32x4 pk; pk.x = cvt_pk_bf16(s[ka][0], s[ka][1]); pk.y = cvt_pk_bf16(s[ka][2], s[ka][3]);
;             if (2 * pp + 1 < 9) { pk.z = cvt_pk_bf16(s[kb][0], s[kb][1]); pk.w = cvt_pk_bf16(s[kb][2], s[kb][3]); } else { pk.z = 0u; pk.w = 0u; }
;             const bf16x8 pf = __builtin_bit_cast(bf16x8, pk);
; #pragma unroll
;             for (int dt = 0; dt < 4; ++dt) { const LAS bf16_t* pa = vbase + ka * (16 * 72) + 16 * dt; const LAS bf16_t* pb = vbase + kb * (16 * 72) + 16 * dt;
;                 oT[dt] = MFMA16(cat8(tr16(pa), tr16(pb)), pf, oT[dt]); } }
	v_mfma_f32_16x16x32_bf16 v[6:9], v[6:9], v[14:17], 0
	s_nop 1
	v_cndmask_b32_e32 v98, v209, v10, vcc
	v_cndmask_b32_e32 v99, v209, v11, vcc
	v_max3_f32 v10, v81, v98, v99
	v_cndmask_b32_e32 v100, v209, v12, vcc
	v_cndmask_b32_e32 v101, v209, v13, vcc
	v_max3_f32 v81, v10, v100, v101
	ds_read_b128 v[10:13], v74 offset:17920
	s_waitcnt lgkmcnt(1)
	v_mfma_f32_16x16x32_bf16 v[6:9], v[28:31], v[18:21], v[6:9]
	s_cmp_gt_i32 s7, 1
	ds_read_b128 v[28:31], v74 offset:17984
	s_cselect_b64 s[10:11], -1, 0
	s_or_b64 vcc, s[42:43], s[10:11]
	s_waitcnt lgkmcnt(1)
	v_mfma_f32_16x16x32_bf16 v[10:13], v[10:13], v[14:17], 0
	s_nop 1
	v_cndmask_b32_e32 v108, v209, v6, vcc
	v_cndmask_b32_e32 v109, v209, v7, vcc
	v_max3_f32 v6, v81, v108, v109
	v_cndmask_b32_e32 v110, v209, v8, vcc
	v_cndmask_b32_e32 v111, v209, v9, vcc
	v_max3_f32 v81, v6, v110, v111
	ds_read_b128 v[6:9], v74 offset:20480
	s_waitcnt lgkmcnt(1)
	v_mfma_f32_16x16x32_bf16 v[28:31], v[28:31], v[18:21], v[10:13]
	s_cmp_gt_i32 s7, 0
	s_cselect_b64 s[10:11], -1, 0
	s_or_b64 vcc, s[42:43], s[10:11]
	ds_read_b128 v[10:13], v74 offset:20544
	s_waitcnt lgkmcnt(1)
	v_mfma_f32_16x16x32_bf16 v[14:17], v[6:9], v[14:17], 0
	s_cmp_lt_u32 s7, 0xfe000000
	s_cselect_b64 s[10:11], -1, 0
	s_or_b64 s[10:11], s[42:43], s[10:11]
	s_waitcnt lgkmcnt(0)
	v_mfma_f32_16x16x32_bf16 v[14:17], v[10:13], v[18:21], v[14:17]
	v_cmp_le_u32_e64 s[44:45], v80, v3
	v_cndmask_b32_e32 v114, v209, v28, vcc
	v_cndmask_b32_e32 v115, v209, v29, vcc
	v_cndmask_b32_e32 v116, v209, v30, vcc
	v_cndmask_b32_e32 v117, v209, v31, vcc
	s_and_b64 vcc, s[10:11], s[44:45]
	v_cmp_lt_u32_e64 s[46:47], v80, v3
	s_nop 0
	v_cndmask_b32_e32 v118, v209, v14, vcc
	s_and_b64 vcc, s[10:11], s[46:47]
	v_cmp_le_u32_e64 s[48:49], v35, v3
	v_max3_f32 v28, v81, v114, v115
	v_cndmask_b32_e32 v15, v209, v15, vcc
	s_and_b64 vcc, s[10:11], s[48:49]
	v_cmp_le_u32_e64 s[50:51], v37, v3
	v_max3_f32 v28, v28, v116, v117
	v_cndmask_b32_e32 v119, v209, v16, vcc
	s_and_b64 vcc, s[10:11], s[50:51]
	v_max3_f32 v14, v28, v118, v15
	v_cndmask_b32_e32 v120, v209, v17, vcc
	v_max3_f32 v3, v14, v119, v120
	ds_bpermute_b32 v14, v83, v3
	v_xor_b32_e32 v16, 32, v202
	v_cmp_lt_i32_e32 vcc, v16, v32
	v_bfe_u32 v5, v2, 2, 2
	v_lshlrev_b32_e32 v2, 3, v2
	v_cndmask_b32_e32 v16, v202, v16, vcc
	s_waitcnt lgkmcnt(0)
	v_max_f32_e32 v14, v14, v14
	v_lshlrev_b32_e32 v85, 2, v16
	v_max_f32_e32 v3, v3, v14
	ds_bpermute_b32 v14, v85, v3
	v_and_b32_e32 v16, 24, v2
	v_or3_b32 v5, v5, v80, s8
	s_movk_i32 s100, 0xa0
	v_mul_lo_u32 v5, v5, s100
	v_add3_u32 v5, s38, v5, v16
	v_add_u32_e32 v197, 0xf000, v5
	s_waitcnt lgkmcnt(0)
	v_max_f32_e32 v2, v14, v14
	v_max_f32_e32 v14, v3, v2
	v_sub_f32_e32 v3, v38, v14
	v_sub_f32_e32 v17, v36, v14
	v_sub_f32_e32 v20, v34, v14
	v_sub_f32_e32 v2, v33, v14
	v_exp_f32_e32 v2, v2
	v_exp_f32_e32 v18, v17
	v_exp_f32_e32 v19, v3
	v_exp_f32_e32 v3, v20
	v_sub_f32_e32 v28, v75, v14
	v_sub_f32_e32 v29, v39, v14
	v_sub_f32_e32 v30, v41, v14
	v_sub_f32_e32 v31, v40, v14
	v_exp_f32_e32 v32, v31
	v_exp_f32_e32 v33, v30
	v_exp_f32_e32 v34, v29
	v_exp_f32_e32 v35, v28
	v_sub_f32_e32 v28, v79, v14
	v_sub_f32_e32 v29, v76, v14
	v_sub_f32_e32 v30, v78, v14
	v_sub_f32_e32 v31, v77, v14
	v_exp_f32_e32 v40, v31
	v_exp_f32_e32 v86, v29
	v_exp_f32_e32 v87, v28
	v_exp_f32_e32 v41, v30
	v_sub_f32_e32 v28, v89, v14
	v_sub_f32_e32 v29, v88, v14
	v_sub_f32_e32 v30, v84, v14
	v_sub_f32_e32 v31, v82, v14
	v_exp_f32_e32 v90, v31
	v_exp_f32_e32 v91, v30
	v_exp_f32_e32 v92, v29
	v_exp_f32_e32 v93, v28
	v_sub_f32_e32 v28, v97, v14
	v_sub_f32_e32 v29, v96, v14
	v_sub_f32_e32 v30, v95, v14
	v_sub_f32_e32 v31, v94, v14
	v_pk_add_f32 v[16:17], v[18:19], 0 op_sel_hi:[1,0]
	v_pk_add_f32 v[20:21], v[2:3], 0 op_sel_hi:[1,0]
	v_exp_f32_e32 v102, v31
	v_exp_f32_e32 v104, v29
	v_exp_f32_e32 v105, v28
	v_exp_f32_e32 v103, v30
	v_pk_add_f32 v[20:21], v[32:33], v[20:21]
	v_pk_add_f32 v[16:17], v[34:35], v[16:17]
	v_pk_add_f32 v[20:21], v[40:41], v[20:21]
	v_pk_add_f32 v[16:17], v[86:87], v[16:17]
	v_pk_add_f32 v[20:21], v[90:91], v[20:21]
	v_pk_add_f32 v[16:17], v[92:93], v[16:17]
	v_sub_f32_e32 v28, v101, v14
	v_pk_add_f32 v[88:89], v[104:105], v[16:17]
	v_pk_add_f32 v[16:17], v[102:103], v[20:21]
	v_sub_f32_e32 v21, v99, v14
	v_sub_f32_e32 v20, v98, v14
	v_exp_f32_e32 v20, v20
	v_exp_f32_e32 v21, v21
	v_sub_f32_e32 v29, v100, v14
	v_exp_f32_e32 v106, v29
	v_exp_f32_e32 v107, v28
	v_pk_add_f32 v[94:95], v[20:21], v[16:17]
	v_sub_f32_e32 v75, v111, v14
	v_sub_f32_e32 v82, v110, v14
	v_cvt_pk_bf16_f32 v16, v2, v3
	v_cvt_pk_bf16_f32 v17, v18, v19
	ds_read_b64_tr_b16 v[30:31], v197 offset:2560
	ds_read_b64_tr_b16 v[28:29], v197
	v_cvt_pk_bf16_f32 v18, v32, v33
	v_cvt_pk_bf16_f32 v19, v34, v35
	ds_read_b64_tr_b16 v[34:35], v197 offset:2592
	ds_read_b64_tr_b16 v[32:33], v197 offset:32
	ds_read_b64_tr_b16 v[36:37], v197 offset:64
	ds_read_b64_tr_b16 v[76:77], v197 offset:96
	ds_read_b64_tr_b16 v[38:39], v197 offset:2624
	ds_read_b64_tr_b16 v[78:79], v197 offset:2656
	v_sub_f32_e32 v3, v109, v14
	v_sub_f32_e32 v2, v108, v14
	v_exp_f32_e32 v2, v2
	v_exp_f32_e32 v108, v82
	v_exp_f32_e32 v109, v75
	v_exp_f32_e32 v3, v3
	v_pk_add_f32 v[88:89], v[106:107], v[88:89]
	s_waitcnt lgkmcnt(6)
	v_mfma_f32_16x16x32_bf16 v[28:31], v[28:31], v[16:19], 0
	v_add_f32_e64 v110, v108, v88
	v_add_f32_e64 v111, v109, v89
	v_pk_add_f32 v[112:113], v[2:3], v[94:95]
	v_add_u32_e32 v81, 0xd800, v5
	s_waitcnt lgkmcnt(4)
	v_mfma_f32_16x16x32_bf16 v[32:35], v[32:35], v[16:19], 0
	v_sub_f32_e32 v75, v117, v14
	v_sub_f32_e32 v82, v116, v14
	v_sub_f32_e32 v15, v15, v14
	s_waitcnt lgkmcnt(1)
; #define GAS __attribute__((address_space(1)))
; #define LAS __attribute__((address_space(3)))
; DI unsigned cvt_pk_bf16(float lo, float hi) { f32x2 v = {lo, hi}; bf16x2_t b = __builtin_convertvector(v, bf16x2_t); return __builtin_bit_cast(unsigned, b); }
; DI unsigned pk4_fp8(float a, float b, float c_, float d) { int w = 0; w = __builtin_amdgcn_cvt_pk_fp8_f32(clamp8(a), clamp8(b), w, false); w = __builtin_amdgcn_cvt_pk_fp8_f32(clamp8(c_), clamp8(d), w, true); return (unsigned)w; }
; DI s16x4 tr16(const LAS void* p) { return __builtin_bit_cast(s16x4, __builtin_amdgcn_ds_read_tr16_b64_v4i16((LAS s16x4*)p)); }
; DI bf16x8 cat8(s16x4 lo, s16x4 hi) { return __builtin_shufflevector(lo, hi, 0, 1, 2, 3, 4, 5, 6, 7); }
; #define MFMA16(a, b, c) __builtin_amdgcn_mfma_f32_16x16x32_bf16((a), (b), (c), 0, 0, 0)
; DI void attn_compute(LAS unsigned char* lds, const Ctx& c, int u, const bf16x8 (&qf)[2][2]) {
;     ...
; #pragma unroll
;         for (int pp = 0; pp < 5; ++pp) { const int ka = 2 * pp, kb = (2 * pp + 1 < 9) ? 2 * pp + 1 : 8;
;             u32x4 pk; pk.x = cvt_pk_bf16(s[ka][0], s[ka][1]); pk.y = cvt_pk_bf16(s[ka][2], s[ka][3]);
;             if (2 * pp + 1 < 9) { pk.z = cvt_pk_bf16(s[kb][0], s[kb][1]); pk.w = cvt_pk_bf16(s[kb][2], s[kb][3]); } else { pk.z = 0u; pk.w = 0u; }
;             const bf16x8 pf = __builtin_bit_cast(bf16x8, pk);
; #pragma unroll
;             for (int dt = 0; dt < 4; ++dt) { const LAS bf16_t* pa = vbase + ka * (16 * 72) + 16 * dt; const LAS bf16_t* pb = vbase + kb * (16 * 72) + 16 * dt;
;                 oT[dt] = MFMA16(cat8(tr16(pa), tr16(pb)), pf, oT[dt]); } }
;         const float inv = 1.0f / lsum; const unsigned tq = tb + (unsigned)dl * (unsigned)(128 * (n + b) + 16 * w + fr), gt = (unsigned)(g * TH) + tq;
;         GAS char* op = (GAS char*)(c.ws + WS_ATTG) + (gt * 512u + (unsigned)(h * 64 + 4 * fq));
; #pragma unroll
;         for (int dt = 0; dt < 4; ++dt) *(GAS unsigned*)(op + 16 * dt) = pk4_fp8(oT[dt][0] * inv, oT[dt][1] * inv, oT[dt][2] * inv, oT[dt][3] * inv);
;         if (fq == 0) *(GAS float*)((GAS char*)(c.ws + WS_LSE) + (gt * 32u + (unsigned)(h * 4))) = m + __builtin_amdgcn_logf(lsum);
	v_mfma_f32_16x16x32_bf16 v[36:39], v[36:39], v[16:19], 0
	v_cmp_eq_u32_e64 s[42:43], 0, v26
	s_waitcnt lgkmcnt(0)
	v_mfma_f32_16x16x32_bf16 v[16:19], v[76:79], v[16:19], 0
	v_cvt_pk_bf16_f32 v77, v86, v87
	ds_read_b64_tr_b16 v[86:87], v197 offset:5120
	ds_read_b64_tr_b16 v[88:89], v197 offset:7680
	v_cvt_pk_bf16_f32 v78, v90, v91
	v_cvt_pk_bf16_f32 v79, v92, v93
	ds_read_b64_tr_b16 v[92:93], v197 offset:7712
	ds_read_b64_tr_b16 v[90:91], v197 offset:5152
	ds_read_b64_tr_b16 v[94:95], v197 offset:5184
	ds_read_b64_tr_b16 v[98:99], v197 offset:5216
	ds_read_b64_tr_b16 v[96:97], v197 offset:7744
	ds_read_b64_tr_b16 v[100:101], v197 offset:7776
	v_cvt_pk_bf16_f32 v76, v40, v41
	v_sub_f32_e32 v41, v115, v14
	v_sub_f32_e32 v40, v114, v14
	s_waitcnt lgkmcnt(6)
	v_mfma_f32_16x16x32_bf16 v[28:31], v[86:89], v[76:79], v[28:31]
	v_exp_f32_e32 v40, v40
	v_exp_f32_e32 v41, v41
	v_exp_f32_e32 v114, v82
	s_waitcnt lgkmcnt(4)
	v_mfma_f32_16x16x32_bf16 v[32:35], v[90:93], v[76:79], v[32:35]
	v_exp_f32_e32 v115, v75
	ds_read_b64_tr_b16 v[86:87], v197 offset:10240
	ds_read_b64_tr_b16 v[88:89], v197 offset:12800
	v_sub_f32_e32 v75, v119, v14
	s_waitcnt lgkmcnt(3)
	v_mfma_f32_16x16x32_bf16 v[36:39], v[94:97], v[76:79], v[36:39]
	v_sub_f32_e32 v82, v118, v14
	v_pk_add_f32 v[112:113], v[40:41], v[112:113]
	s_waitcnt lgkmcnt(2)
	v_mfma_f32_16x16x32_bf16 v[16:19], v[98:101], v[76:79], v[16:19]
	ds_read_b64_tr_b16 v[92:93], v197 offset:12832
	ds_read_b64_tr_b16 v[90:91], v197 offset:10272
	ds_read_b64_tr_b16 v[94:95], v197 offset:10304
	ds_read_b64_tr_b16 v[98:99], v197 offset:10336
	ds_read_b64_tr_b16 v[96:97], v197 offset:12864
	ds_read_b64_tr_b16 v[100:101], v197 offset:12896
	v_sub_f32_e32 v5, v120, v14
	v_cvt_pk_bf16_f32 v77, v104, v105
	v_cvt_pk_bf16_f32 v79, v106, v107
	v_exp_f32_e32 v104, v82
	v_exp_f32_e32 v105, v15
	v_exp_f32_e32 v106, v75
	v_exp_f32_e32 v107, v5
	v_cvt_pk_bf16_f32 v76, v102, v103
	v_cvt_pk_bf16_f32 v78, v20, v21
	v_pk_add_f32 v[20:21], v[114:115], v[110:111]
	v_lshl_add_u32 v82, s6, 7, v27
	s_waitcnt lgkmcnt(6)
	v_mfma_f32_16x16x32_bf16 v[28:31], v[86:89], v[76:79], v[28:31]
	ds_read_b64_tr_b16 v[86:87], v197 offset:15360
	ds_read_b64_tr_b16 v[88:89], v197 offset:17920
	v_mov_b32_e32 v27, v4
	s_waitcnt lgkmcnt(6)
	v_mfma_f32_16x16x32_bf16 v[32:35], v[90:93], v[76:79], v[32:35]
	s_waitcnt lgkmcnt(3)
	v_mfma_f32_16x16x32_bf16 v[36:39], v[94:97], v[76:79], v[36:39]
	s_waitcnt lgkmcnt(2)
	v_mfma_f32_16x16x32_bf16 v[16:19], v[98:101], v[76:79], v[16:19]
	v_cvt_pk_bf16_f32 v76, v2, v3
	v_pk_add_f32 v[2:3], v[106:107], v[20:21]
	v_pk_add_f32 v[20:21], v[104:105], v[112:113]
	v_add_f32_e32 v2, v2, v3
	v_add_f32_e32 v5, v20, v21
	v_add_f32_e32 v15, v5, v2
	ds_bpermute_b32 v20, v83, v15
	ds_read_b64_tr_b16 v[92:93], v197 offset:17952
	ds_read_b64_tr_b16 v[90:91], v197 offset:15392
	ds_read_b64_tr_b16 v[94:95], v197 offset:15424
	ds_read_b64_tr_b16 v[98:99], v197 offset:15456
	ds_read_b64_tr_b16 v[96:97], v197 offset:17984
	ds_read_b64_tr_b16 v[100:101], v197 offset:18016
	v_cvt_pk_bf16_f32 v77, v108, v109
	v_cvt_pk_bf16_f32 v78, v40, v41
	v_cvt_pk_bf16_f32 v79, v114, v115
	s_waitcnt lgkmcnt(6)
	v_add_f32_e32 v15, v15, v20
	ds_bpermute_b32 v20, v85, v15
	v_mfma_f32_16x16x32_bf16 v[28:31], v[86:89], v[76:79], v[28:31]
	ds_read_b64_tr_b16 v[86:87], v197 offset:20480
	v_cvt_pk_bf16_f32 v2, v104, v105
	v_cvt_pk_bf16_f32 v3, v106, v107
	s_waitcnt lgkmcnt(6)
	v_mfma_f32_16x16x32_bf16 v[32:35], v[90:93], v[76:79], v[32:35]
	s_waitcnt lgkmcnt(1)
	v_add_f32_e32 v15, v15, v20
	s_waitcnt lgkmcnt(0)
	v_mov_b32_e32 v88, v86
	v_mov_b32_e32 v89, v87
	v_mfma_f32_16x16x32_bf16 v[36:39], v[94:97], v[76:79], v[36:39]
	ds_read_b64_tr_b16 v[90:91], v197 offset:20512
	ds_read_b64_tr_b16 v[94:95], v197 offset:20544
	ds_read_b64_tr_b16 v[102:103], v197 offset:20576
	v_div_scale_f32 v20, s[8:9], v15, v15, 1.0
	s_waitcnt lgkmcnt(2)
	v_mov_b32_e32 v92, v90
	v_mov_b32_e32 v93, v91
	s_waitcnt lgkmcnt(1)
	v_mov_b32_e32 v96, v94
	v_mov_b32_e32 v97, v95
	s_waitcnt lgkmcnt(0)
	v_mov_b32_e32 v104, v102
	v_mov_b32_e32 v105, v103
	v_mfma_f32_16x16x32_bf16 v[16:19], v[98:101], v[76:79], v[16:19]
	v_rcp_f32_e32 v21, v20
	v_mov_b32_e32 v5, v4
	s_nop 1
	v_mfma_f32_16x16x32_bf16 v[28:31], v[86:89], v[2:5], v[28:31]
	v_mfma_f32_16x16x32_bf16 v[32:35], v[90:93], v[2:5], v[32:35]
	v_mfma_f32_16x16x32_bf16 v[36:39], v[94:97], v[2:5], v[36:39]
	v_mfma_f32_16x16x32_bf16 v[16:19], v[102:105], v[2:5], v[16:19]
	v_fma_f32 v2, -v20, v21, 1.0
	v_fmac_f32_e32 v21, v2, v21
	v_div_scale_f32 v2, vcc, 1.0, v15, 1.0
	v_mul_f32_e32 v3, v2, v21
	v_fma_f32 v5, -v20, v3, v2
	v_fmac_f32_e32 v3, v5, v21
	v_fma_f32 v2, -v20, v3, v2
	v_div_fmas_f32 v2, v2, v21, v3
	v_div_fixup_f32 v3, v2, v15, 1.0
	v_mul_f32_e32 v20, v3, v28
	v_mul_f32_e32 v21, v3, v29
	v_med3_f32 v20, v20, s35, v225
	v_med3_f32 v21, v21, s35, v225
	v_cvt_pk_fp8_f32 v27, v20, v21
	v_mul_f32_e32 v26, v3, v30
	v_mul_f32_e32 v20, v3, v31
	v_med3_f32 v21, v26, s35, v225
	v_med3_f32 v20, v20, s35, v225
	v_cvt_pk_fp8_f32 v27, v21, v20 op_sel:[0,0,1]
	v_mul_f32_e32 v20, v3, v32
	v_mul_f32_e32 v21, v3, v33
	v_med3_f32 v20, v20, s35, v225
	v_med3_f32 v21, v21, s35, v225
	v_mov_b32_e32 v28, v4
	v_cvt_pk_fp8_f32 v28, v20, v21
	v_mul_f32_e32 v26, v3, v34
	v_mul_f32_e32 v20, v3, v35
	v_med3_f32 v21, v26, s35, v225
	v_med3_f32 v20, v20, s35, v225
	v_cvt_pk_fp8_f32 v28, v21, v20 op_sel:[0,0,1]
	v_mul_f32_e32 v20, v3, v36
	v_mul_f32_e32 v21, v3, v37
	v_med3_f32 v20, v20, s35, v225
	v_med3_f32 v21, v21, s35, v225
	v_mov_b32_e32 v29, v4
	v_cvt_pk_fp8_f32 v29, v20, v21
	v_mul_f32_e32 v26, v3, v38
	v_mul_f32_e32 v20, v3, v39
	v_med3_f32 v21, v26, s35, v225
	v_med3_f32 v20, v20, s35, v225
	v_mul_f32_e32 v16, v3, v16
	v_mul_f32_e32 v17, v3, v17
	v_cvt_pk_fp8_f32 v29, v21, v20 op_sel:[0,0,1]
	v_med3_f32 v16, v16, s35, v225
	v_med3_f32 v17, v17, s35, v225
	v_mov_b32_e32 v20, v4
	v_cvt_pk_fp8_f32 v20, v16, v17
	v_lshlrev_b32_e32 v2, s81, v82
	v_add_u32_e32 v2, s83, v2
	v_mul_f32_e32 v18, v3, v18
	v_mul_f32_e32 v3, v3, v19
	v_lshlrev_b32_e32 v5, 9, v2
	v_med3_f32 v16, v18, s35, v225
	v_med3_f32 v3, v3, s35, v225
	v_or3_b32 v5, v5, s82, v80
	v_cvt_pk_fp8_f32 v20, v16, v3 op_sel:[0,0,1]
	global_store_dword v5, v27, s[60:61]
	global_store_dword v5, v28, s[60:61] offset:16
	global_store_dword v5, v29, s[60:61] offset:32
	global_store_dword v5, v20, s[60:61] offset:48
	s_and_saveexec_b64 s[66:67], s[42:43]
	s_cbranch_execz .LBB0_695
	v_log_f32_e32 v3, v15
	v_lshl_or_b32 v2, v2, 5, s80
	v_add_f32_e32 v3, v14, v3
	global_store_dword v2, v3, s[30:31]
; #define LAS __attribute__((address_space(3)))
; DI void attn_compute(LAS unsigned char* lds, const Ctx& c, int u, const bf16x8 (&qf)[2][2]) {
;     ...
; #pragma unroll
;     for (int b = 0; b < 2; ++b) {
;         const int kt0 = 8 * b + w;
;         const LAS bf16_t* kbase = Ks + (16 * w + fr) * 72 + 8 * fq + b * (128 * 72);
;         const LAS bf16_t* vbase = Vs + (16 * w + 4 * fq + (fr >> 2)) * 72 + (fr & 3) * 4 + b * (128 * 72);
;         f32x4 s[9]; float m = -1e30f;
; #pragma unroll
;         for (int kr = 0; kr < 9; ++kr) { const int kt = kt0 + kr; f32x4 a = (f32x4){0.f, 0.f, 0.f, 0.f};
; #pragma unroll
;             for (int d0 = 0; d0 < 2; ++d0) { const bf16x8 af = *(const LAS bf16x8*)(kbase + kr * (16 * 72) + 32 * d0); a = MFMA16(af, qf[b][d0], a); }
; #pragma unroll
;             for (int rg = 0; rg < 4; ++rg) { const bool tile_ok = (b > 0) || (n > 0) || (kt >= 8);
;                 bool ok = tile_ok; if (kr == 0) ok = ok && (4 * fq + rg >= fr); if (kr == 8) ok = ok && (4 * fq + rg <= fr);
;                 a[rg] = ok ? a[rg] : -1e30f; m = fmaxf(m, a[rg]); }
;             s[kr] = a; }
;         m = fmaxf(m, __shfl_xor(m, 16)); m = fmaxf(m, __shfl_xor(m, 32));
;         f32x4 ls4 = (f32x4){0.f, 0.f, 0.f, 0.f}; const f32x4 m4 = (f32x4){m, m, m, m};
; #pragma unroll
;         for (int kr = 0; kr < 9; ++kr) { const f32x4 d = s[kr] - m4;
;             s[kr] = (f32x4){__builtin_amdgcn_exp2f(d[0]), __builtin_amdgcn_exp2f(d[1]), __builtin_amdgcn_exp2f(d[2]), __builtin_amdgcn_exp2f(d[3])}; ls4 += s[kr]; }
;         float lsum = (ls4[0] + ls4[1]) + (ls4[2] + ls4[3]);
;         lsum += __shfl_xor(lsum, 16); lsum += __shfl_xor(lsum, 32);
;         f32x4 oT[4];
; #pragma unroll
;         for (int dt = 0; dt < 4; ++dt) oT[dt] = (f32x4){0.f, 0.f, 0.f, 0.f};
; #pragma unroll
;         for (int pp = 0; pp < 5; ++pp) { const int ka = 2 * pp, kb = (2 * pp + 1 < 9) ? 2 * pp + 1 : 8;
;             u32x4 pk; pk.x = cvt_pk_bf16(s[ka][0], s[ka][1]); pk.y = cvt_pk_bf16(s[ka][2], s[ka][3]);
;             if (2 * pp + 1 < 9) { pk.z = cvt_pk_bf16(s[kb][0], s[kb][1]); pk.w = cvt_pk_bf16(s[kb][2], s[kb][3]); } else { pk.z = 0u; pk.w = 0u; }
;             const bf16x8 pf = __builtin_bit_cast(bf16x8, pk);
; #pragma unroll
;             for (int dt = 0; dt < 4; ++dt) { const LAS bf16_t* pa = vbase + ka * (16 * 72) + 16 * dt; const LAS bf16_t* pb = vbase + kb * (16 * 72) + 16 * dt;
.LBB0_695:
	s_or_b64 exec, exec, s[66:67]
	v_cvt_pk_f32_fp8_e32 v[2:3], v24
	v_cvt_pk_f32_fp8_sdwa v[14:15], v24 src0_sel:WORD_1
	v_cvt_pk_f32_fp8_e32 v[16:17], v25
	v_cvt_pk_f32_fp8_sdwa v[24:25], v25 src0_sel:WORD_1
	v_cvt_pk_bf16_f32 v18, v2, v3
	v_cvt_pk_bf16_f32 v19, v14, v15
	v_cvt_pk_bf16_f32 v20, v16, v17
	v_cvt_pk_bf16_f32 v21, v24, v25
	v_cvt_pk_f32_fp8_e32 v[2:3], v22
	v_cvt_pk_f32_fp8_sdwa v[16:17], v22 src0_sel:WORD_1
	v_cvt_pk_f32_fp8_e32 v[24:25], v23
	v_cvt_pk_f32_fp8_sdwa v[22:23], v23 src0_sel:WORD_1
	v_mfma_f32_16x16x32_bf16 v[6:9], v[6:9], v[18:21], 0
	v_cvt_pk_bf16_f32 v14, v2, v3
	v_cvt_pk_bf16_f32 v15, v16, v17
	v_cvt_pk_bf16_f32 v16, v24, v25
	v_cvt_pk_bf16_f32 v17, v22, v23
	s_mov_b32 s6, 0xf149f2ca
	ds_read_b128 v[22:25], v74 offset:25664
	v_mfma_f32_16x16x32_bf16 v[6:9], v[10:13], v[14:17], v[6:9]
	ds_read_b128 v[10:13], v74 offset:23104
	ds_read_b128 v[26:29], v74 offset:28224
	ds_read_b128 v[30:33], v74 offset:30784
	ds_read_b128 v[34:37], v74 offset:33344
	ds_read_b128 v[38:41], v74 offset:35904
	s_nop 2
	v_cndmask_b32_e64 v2, v209, v6, s[52:53]
	v_cndmask_b32_e64 v3, v209, v7, s[54:55]
	v_cndmask_b32_e64 v86, v209, v8, s[56:57]
	v_cndmask_b32_e64 v87, v209, v9, s[58:59]
	ds_read_b128 v[6:9], v74 offset:23040
	s_waitcnt lgkmcnt(0)
	v_mfma_f32_16x16x32_bf16 v[6:9], v[6:9], v[18:21], 0
	v_max3_f32 v5, v2, s6, v3
	v_max3_f32 v5, v5, v86, v87
	ds_read_b128 v[76:79], v74 offset:38464
	v_mfma_f32_16x16x32_bf16 v[6:9], v[10:13], v[14:17], v[6:9]
	ds_read_b128 v[10:13], v74 offset:25600
	s_waitcnt lgkmcnt(0)
	v_mfma_f32_16x16x32_bf16 v[10:13], v[10:13], v[18:21], 0
	s_nop 4
	v_max3_f32 v5, v5, v6, v7
	v_max3_f32 v5, v5, v8, v9
	v_mfma_f32_16x16x32_bf16 v[10:13], v[22:25], v[14:17], v[10:13]
	ds_read_b128 v[22:25], v74 offset:28160
	s_waitcnt lgkmcnt(0)
	v_mfma_f32_16x16x32_bf16 v[22:25], v[22:25], v[18:21], 0
	s_nop 4
	v_max3_f32 v5, v5, v10, v11
	v_max3_f32 v5, v5, v12, v13
	v_mfma_f32_16x16x32_bf16 v[22:25], v[26:29], v[14:17], v[22:25]
	ds_read_b128 v[26:29], v74 offset:30720
	s_waitcnt lgkmcnt(0)
	v_mfma_f32_16x16x32_bf16 v[26:29], v[26:29], v[18:21], 0
	s_nop 4
	v_max3_f32 v5, v5, v22, v23
	v_max3_f32 v5, v5, v24, v25
	v_mfma_f32_16x16x32_bf16 v[26:29], v[30:33], v[14:17], v[26:29]
	ds_read_b128 v[30:33], v74 offset:33280
	s_waitcnt lgkmcnt(0)
	v_mfma_f32_16x16x32_bf16 v[30:33], v[30:33], v[18:21], 0
	s_nop 4
	v_max3_f32 v5, v5, v26, v27
	v_max3_f32 v5, v5, v28, v29
	v_mfma_f32_16x16x32_bf16 v[30:33], v[34:37], v[14:17], v[30:33]
	ds_read_b128 v[34:37], v74 offset:35840
	s_waitcnt lgkmcnt(0)
	v_mfma_f32_16x16x32_bf16 v[34:37], v[34:37], v[18:21], 0
	s_nop 4
	v_max3_f32 v5, v5, v30, v31
	v_max3_f32 v5, v5, v32, v33
	v_mfma_f32_16x16x32_bf16 v[34:37], v[38:41], v[14:17], v[34:37]
	ds_read_b128 v[38:41], v74 offset:38400
	s_waitcnt lgkmcnt(0)
	v_mfma_f32_16x16x32_bf16 v[38:41], v[38:41], v[18:21], 0
	s_nop 4
	v_max3_f32 v5, v5, v34, v35
	v_max3_f32 v5, v5, v36, v37
	v_mfma_f32_16x16x32_bf16 v[38:41], v[76:79], v[14:17], v[38:41]
	ds_read_b128 v[76:79], v74 offset:40960
	s_waitcnt lgkmcnt(0)
	v_mfma_f32_16x16x32_bf16 v[18:21], v[76:79], v[18:21], 0
	ds_read_b128 v[74:77], v74 offset:41024
	s_nop 3
	v_max3_f32 v5, v5, v38, v39
	v_max3_f32 v5, v5, v40, v41
	s_waitcnt lgkmcnt(0)
	v_mfma_f32_16x16x32_bf16 v[14:17], v[74:77], v[14:17], v[18:21]
	s_nop 7
	v_cndmask_b32_e64 v94, v209, v14, s[44:45]
	v_cndmask_b32_e64 v95, v209, v15, s[46:47]
	v_max3_f32 v5, v5, v94, v95
	v_cndmask_b32_e64 v96, v209, v16, s[48:49]
	v_cndmask_b32_e64 v97, v209, v17, s[50:51]
	v_max3_f32 v5, v5, v96, v97
	ds_bpermute_b32 v14, v83, v5
	s_waitcnt lgkmcnt(0)
	v_max_f32_e32 v14, v14, v14
	v_max_f32_e32 v5, v5, v14
	ds_bpermute_b32 v14, v85, v5
	s_waitcnt lgkmcnt(0)
	v_max_f32_e32 v14, v14, v14
	v_max_f32_e32 v84, v5, v14
	v_sub_f32_e32 v5, v87, v84
	v_sub_f32_e32 v14, v86, v84
	v_sub_f32_e32 v3, v3, v84
	v_sub_f32_e32 v2, v2, v84
	v_exp_f32_e32 v86, v2
	v_exp_f32_e32 v87, v3
	v_exp_f32_e32 v88, v14
	v_exp_f32_e32 v89, v5
	v_sub_f32_e32 v5, v9, v84
	v_sub_f32_e32 v8, v8, v84
	v_sub_f32_e32 v7, v7, v84
	v_sub_f32_e32 v6, v6, v84
	v_exp_f32_e32 v90, v6
	v_exp_f32_e32 v91, v7
	v_exp_f32_e32 v92, v8
	v_exp_f32_e32 v93, v5
	v_sub_f32_e32 v5, v13, v84
	v_sub_f32_e32 v8, v12, v84
	v_sub_f32_e32 v9, v11, v84
	v_sub_f32_e32 v10, v10, v84
	v_exp_f32_e32 v74, v10
	v_exp_f32_e32 v75, v9
	v_exp_f32_e32 v76, v8
	v_exp_f32_e32 v77, v5
	v_sub_f32_e32 v5, v25, v84
	v_sub_f32_e32 v8, v24, v84
	v_sub_f32_e32 v9, v23, v84
	v_sub_f32_e32 v10, v22, v84
	v_exp_f32_e32 v24, v10
	v_exp_f32_e32 v25, v9
	v_exp_f32_e32 v78, v8
	v_exp_f32_e32 v79, v5
	v_sub_f32_e32 v5, v29, v84
	v_sub_f32_e32 v8, v28, v84
	v_sub_f32_e32 v9, v27, v84
	v_sub_f32_e32 v10, v26, v84
	v_pk_add_f32 v[2:3], v[88:89], 0 op_sel_hi:[1,0]
	v_pk_add_f32 v[14:15], v[86:87], 0 op_sel_hi:[1,0]
	v_exp_f32_e32 v16, v10
	v_exp_f32_e32 v17, v9
	v_exp_f32_e32 v18, v8
	v_exp_f32_e32 v19, v5
	v_sub_f32_e32 v5, v33, v84
	v_sub_f32_e32 v8, v32, v84
	v_sub_f32_e32 v9, v31, v84
	v_sub_f32_e32 v10, v30, v84
	v_pk_add_f32 v[6:7], v[90:91], v[14:15]
	v_pk_add_f32 v[2:3], v[92:93], v[2:3]
	v_exp_f32_e32 v20, v10
	v_exp_f32_e32 v21, v9
	v_exp_f32_e32 v22, v8
	v_exp_f32_e32 v23, v5
	v_sub_f32_e32 v5, v37, v84
	v_sub_f32_e32 v10, v36, v84
	v_sub_f32_e32 v9, v35, v84
	v_sub_f32_e32 v8, v34, v84
	v_pk_add_f32 v[2:3], v[76:77], v[2:3]
	v_pk_add_f32 v[6:7], v[74:75], v[6:7]
	v_exp_f32_e32 v8, v8
	v_exp_f32_e32 v9, v9
	v_exp_f32_e32 v10, v10
	v_exp_f32_e32 v11, v5
	v_sub_f32_e32 v5, v41, v84
	v_sub_f32_e32 v14, v40, v84
	v_sub_f32_e32 v13, v39, v84
	v_sub_f32_e32 v12, v38, v84
	v_pk_add_f32 v[6:7], v[24:25], v[6:7]
	v_pk_add_f32 v[2:3], v[78:79], v[2:3]
	v_exp_f32_e32 v12, v12
	v_exp_f32_e32 v13, v13
	v_exp_f32_e32 v14, v14
	v_exp_f32_e32 v15, v5
	v_pk_add_f32 v[2:3], v[18:19], v[2:3]
	v_pk_add_f32 v[6:7], v[16:17], v[6:7]
	v_pk_add_f32 v[2:3], v[22:23], v[2:3]
	v_pk_add_f32 v[6:7], v[20:21], v[6:7]
	v_pk_add_f32 v[2:3], v[10:11], v[2:3]
	v_pk_add_f32 v[6:7], v[8:9], v[6:7]
	v_pk_add_f32 v[28:29], v[14:15], v[2:3]
	v_pk_add_f32 v[26:27], v[12:13], v[6:7]
	v_sub_f32_e32 v5, v97, v84
	v_sub_f32_e32 v6, v96, v84
	v_sub_f32_e32 v3, v95, v84
	v_sub_f32_e32 v2, v94, v84
	v_exp_f32_e32 v2, v2
	v_exp_f32_e32 v3, v3
	v_exp_f32_e32 v6, v6
	v_exp_f32_e32 v7, v5
	ds_read_b64_tr_b16 v[34:35], v197 offset:23040
	ds_read_b64_tr_b16 v[32:33], v197 offset:20480
	ds_read_b64_tr_b16 v[36:37], v197 offset:20512
	ds_read_b64_tr_b16 v[38:39], v197 offset:23072
	v_pk_add_f32 v[26:27], v[2:3], v[26:27]
	v_pk_add_f32 v[28:29], v[6:7], v[28:29]
	v_add_f32_e32 v5, v26, v27
	v_add_f32_e32 v26, v28, v29
	v_cvt_pk_bf16_f32 v28, v86, v87
	v_cvt_pk_bf16_f32 v29, v88, v89
	v_cvt_pk_bf16_f32 v30, v90, v91
	v_cvt_pk_bf16_f32 v31, v92, v93
	ds_read_b64_tr_b16 v[86:87], v197 offset:20544
	ds_read_b64_tr_b16 v[88:89], v197 offset:23104
	ds_read_b64_tr_b16 v[90:91], v197 offset:20576
	ds_read_b64_tr_b16 v[92:93], v197 offset:23136
	s_waitcnt lgkmcnt(6)
; #define GAS __attribute__((address_space(1)))
; #define LAS __attribute__((address_space(3)))
; DI unsigned cvt_pk_bf16(float lo, float hi) { f32x2 v = {lo, hi}; bf16x2_t b = __builtin_convertvector(v, bf16x2_t); return __builtin_bit_cast(unsigned, b); }
; DI unsigned pk4_fp8(float a, float b, float c_, float d) { int w = 0; w = __builtin_amdgcn_cvt_pk_fp8_f32(clamp8(a), clamp8(b), w, false); w = __builtin_amdgcn_cvt_pk_fp8_f32(clamp8(c_), clamp8(d), w, true); return (unsigned)w; }
; DI s16x4 tr16(const LAS void* p) { return __builtin_bit_cast(s16x4, __builtin_amdgcn_ds_read_tr16_b64_v4i16((LAS s16x4*)p)); }
; DI bf16x8 cat8(s16x4 lo, s16x4 hi) { return __builtin_shufflevector(lo, hi, 0, 1, 2, 3, 4, 5, 6, 7); }
; #define MFMA16(a, b, c) __builtin_amdgcn_mfma_f32_16x16x32_bf16((a), (b), (c), 0, 0, 0)
; DI void attn_compute(LAS unsigned char* lds, const Ctx& c, int u, const bf16x8 (&qf)[2][2]) {
;     ...
; #pragma unroll
;         for (int pp = 0; pp < 5; ++pp) { const int ka = 2 * pp, kb = (2 * pp + 1 < 9) ? 2 * pp + 1 : 8;
;             u32x4 pk; pk.x = cvt_pk_bf16(s[ka][0], s[ka][1]); pk.y = cvt_pk_bf16(s[ka][2], s[ka][3]);
;             if (2 * pp + 1 < 9) { pk.z = cvt_pk_bf16(s[kb][0], s[kb][1]); pk.w = cvt_pk_bf16(s[kb][2], s[kb][3]); } else { pk.z = 0u; pk.w = 0u; }
;             const bf16x8 pf = __builtin_bit_cast(bf16x8, pk);
; #pragma unroll
;             for (int dt = 0; dt < 4; ++dt) { const LAS bf16_t* pa = vbase + ka * (16 * 72) + 16 * dt; const LAS bf16_t* pb = vbase + kb * (16 * 72) + 16 * dt;
;                 oT[dt] = MFMA16(cat8(tr16(pa), tr16(pb)), pf, oT[dt]); } }
;         const float inv = 1.0f / lsum; const unsigned tq = tb + (unsigned)dl * (unsigned)(128 * (n + b) + 16 * w + fr), gt = (unsigned)(g * TH) + tq;
;         GAS char* op = (GAS char*)(c.ws + WS_ATTG) + (gt * 512u + (unsigned)(h * 64 + 4 * fq));
; #pragma unroll
;         for (int dt = 0; dt < 4; ++dt) *(GAS unsigned*)(op + 16 * dt) = pk4_fp8(oT[dt][0] * inv, oT[dt][1] * inv, oT[dt][2] * inv, oT[dt][3] * inv);
;         if (fq == 0) *(GAS float*)((GAS char*)(c.ws + WS_LSE) + (gt * 32u + (unsigned)(h * 4))) = m + __builtin_amdgcn_logf(lsum);
	v_mfma_f32_16x16x32_bf16 v[32:35], v[32:35], v[28:31], 0
	v_cvt_pk_bf16_f32 v74, v74, v75
	v_cvt_pk_bf16_f32 v75, v76, v77
	v_cvt_pk_bf16_f32 v76, v24, v25
	s_waitcnt lgkmcnt(4)
	v_mfma_f32_16x16x32_bf16 v[36:39], v[36:39], v[28:31], 0
	v_cvt_pk_bf16_f32 v77, v78, v79
	v_cvt_pk_bf16_f32 v16, v16, v17
	v_cvt_pk_bf16_f32 v17, v18, v19
	s_waitcnt lgkmcnt(2)
	v_mfma_f32_16x16x32_bf16 v[86:89], v[86:89], v[28:31], 0
	v_cvt_pk_bf16_f32 v18, v20, v21
	v_cvt_pk_bf16_f32 v19, v22, v23
	v_cvt_pk_bf16_f32 v8, v8, v9
	s_waitcnt lgkmcnt(0)
	v_mfma_f32_16x16x32_bf16 v[28:31], v[90:93], v[28:31], 0
	ds_read_b64_tr_b16 v[90:91], v197 offset:25600
	ds_read_b64_tr_b16 v[92:93], v197 offset:28160
	v_cvt_pk_bf16_f32 v9, v10, v11
	v_cvt_pk_bf16_f32 v10, v12, v13
	s_waitcnt lgkmcnt(0)
	v_mfma_f32_16x16x32_bf16 v[32:35], v[90:93], v[74:77], v[32:35]
	ds_read_b64_tr_b16 v[90:91], v197 offset:25632
	ds_read_b64_tr_b16 v[92:93], v197 offset:28192
	v_cvt_pk_bf16_f32 v11, v14, v15
	v_add_f32_e32 v5, v5, v26
	s_waitcnt lgkmcnt(0)
	v_mfma_f32_16x16x32_bf16 v[36:39], v[90:93], v[74:77], v[36:39]
	ds_read_b64_tr_b16 v[90:91], v197 offset:25664
	ds_read_b64_tr_b16 v[92:93], v197 offset:28224
	ds_bpermute_b32 v26, v83, v5
	v_cvt_pk_bf16_f32 v2, v2, v3
	s_waitcnt lgkmcnt(1)
	v_mfma_f32_16x16x32_bf16 v[86:89], v[90:93], v[74:77], v[86:89]
	ds_read_b64_tr_b16 v[90:91], v197 offset:25696
	ds_read_b64_tr_b16 v[92:93], v197 offset:28256
	ds_read_b64_tr_b16 v[20:21], v197 offset:30720
	ds_read_b64_tr_b16 v[22:23], v197 offset:33280
	s_waitcnt lgkmcnt(4)
	v_add_f32_e32 v26, v5, v26
	s_waitcnt lgkmcnt(0)
	v_mfma_f32_16x16x32_bf16 v[20:23], v[20:23], v[16:19], v[32:35]
	s_nop 2
	ds_read_b64_tr_b16 v[32:33], v197 offset:30752
	ds_read_b64_tr_b16 v[34:35], v197 offset:33312
	v_cvt_pk_bf16_f32 v3, v6, v7
	v_mov_b32_e32 v5, v4
	v_mfma_f32_16x16x32_bf16 v[28:31], v[90:93], v[74:77], v[28:31]
	ds_bpermute_b32 v27, v85, v26
	s_waitcnt lgkmcnt(1)
	v_mfma_f32_16x16x32_bf16 v[32:35], v[32:35], v[16:19], v[36:39]
	s_nop 2
	ds_read_b64_tr_b16 v[36:37], v197 offset:30784
	ds_read_b64_tr_b16 v[38:39], v197 offset:33344
	ds_read_b64_tr_b16 v[74:75], v197 offset:30816
	ds_read_b64_tr_b16 v[76:77], v197 offset:33376
	ds_read_b64_tr_b16 v[12:13], v197 offset:35840
	ds_read_b64_tr_b16 v[14:15], v197 offset:38400
	s_waitcnt lgkmcnt(0)
	v_mfma_f32_16x16x32_bf16 v[12:15], v[12:15], v[8:11], v[20:23]
	s_nop 2
	ds_read_b64_tr_b16 v[20:21], v197 offset:35872
	ds_read_b64_tr_b16 v[22:23], v197 offset:38432
	v_mfma_f32_16x16x32_bf16 v[36:39], v[36:39], v[16:19], v[86:89]
	v_mfma_f32_16x16x32_bf16 v[16:19], v[74:77], v[16:19], v[28:31]
	s_nop 2
	ds_read_b64_tr_b16 v[28:29], v197 offset:35904
	ds_read_b64_tr_b16 v[30:31], v197 offset:38464
	s_waitcnt lgkmcnt(2)
	v_mfma_f32_16x16x32_bf16 v[20:23], v[20:23], v[8:11], v[32:35]
	s_nop 2
	ds_read_b64_tr_b16 v[32:33], v197 offset:35936
	ds_read_b64_tr_b16 v[34:35], v197 offset:38496
	s_waitcnt lgkmcnt(2)
	v_mfma_f32_16x16x32_bf16 v[28:31], v[28:31], v[8:11], v[36:39]
	s_waitcnt lgkmcnt(0)
	v_mfma_f32_16x16x32_bf16 v[8:11], v[32:35], v[8:11], v[16:19]
	s_nop 2
	ds_read_b64_tr_b16 v[16:17], v197 offset:40960
	s_waitcnt lgkmcnt(0)
	v_mov_b32_e32 v18, v16
	v_mov_b32_e32 v19, v17
	s_nop 1
	v_mfma_f32_16x16x32_bf16 v[12:15], v[16:19], v[2:5], v[12:15]
	ds_read_b64_tr_b16 v[16:17], v197 offset:40992
	s_waitcnt lgkmcnt(0)
	v_mov_b32_e32 v18, v16
	v_mov_b32_e32 v19, v17
	s_nop 1
	v_mfma_f32_16x16x32_bf16 v[16:19], v[16:19], v[2:5], v[20:23]
	s_nop 2
	ds_read_b64_tr_b16 v[20:21], v197 offset:41024
	s_waitcnt lgkmcnt(0)
	v_mov_b32_e32 v22, v20
	v_mov_b32_e32 v23, v21
	s_nop 1
	v_mfma_f32_16x16x32_bf16 v[20:23], v[20:23], v[2:5], v[28:31]
	s_nop 2
	ds_read_b64_tr_b16 v[28:29], v197 offset:41056
	s_waitcnt lgkmcnt(0)
	v_mov_b32_e32 v30, v28
	v_mov_b32_e32 v31, v29
	s_nop 1
	v_mfma_f32_16x16x32_bf16 v[6:9], v[28:31], v[2:5], v[8:11]
	v_add_f32_e32 v2, v26, v27
	v_div_scale_f32 v3, s[6:7], v2, v2, 1.0
	v_rcp_f32_e32 v5, v3
	s_nop 0
	v_fma_f32 v10, -v3, v5, 1.0
	v_fmac_f32_e32 v5, v10, v5
	v_div_scale_f32 v10, vcc, 1.0, v2, 1.0
	v_mul_f32_e32 v11, v10, v5
	v_fma_f32 v24, -v3, v11, v10
	v_fmac_f32_e32 v11, v24, v5
	v_fma_f32 v3, -v3, v11, v10
	v_div_fmas_f32 v3, v3, v5, v11
	v_div_fixup_f32 v5, v3, v2, 1.0
	v_mul_f32_e32 v11, v5, v12
	v_mul_f32_e32 v12, v5, v13
	v_mul_f32_e32 v13, v5, v14
	v_mul_f32_e32 v14, v5, v15
	v_med3_f32 v11, v11, s35, v225
	v_med3_f32 v12, v12, s35, v225
	v_mov_b32_e32 v15, v4
	v_cvt_pk_fp8_f32 v15, v11, v12
	v_add_u32_e32 v3, 0x80, v82
	v_med3_f32 v11, v13, s35, v225
	v_med3_f32 v12, v14, s35, v225
	v_lshlrev_b32_e32 v3, s81, v3
	v_cvt_pk_fp8_f32 v15, v11, v12 op_sel:[0,0,1]
	v_add_u32_e32 v3, s83, v3
	v_lshlrev_b32_e32 v10, 9, v3
	v_or3_b32 v10, v10, s82, v80
	v_mul_f32_e32 v11, v5, v16
	v_mul_f32_e32 v12, v5, v17
	global_store_dword v10, v15, s[60:61]
	v_med3_f32 v11, v11, s35, v225
	v_med3_f32 v12, v12, s35, v225
	v_mov_b32_e32 v15, v4
	v_cvt_pk_fp8_f32 v15, v11, v12
	v_mul_f32_e32 v13, v5, v18
	v_mul_f32_e32 v14, v5, v19
	v_med3_f32 v11, v13, s35, v225
	v_med3_f32 v12, v14, s35, v225
	v_cvt_pk_fp8_f32 v15, v11, v12 op_sel:[0,0,1]
	v_mul_f32_e32 v11, v5, v20
	v_mul_f32_e32 v12, v5, v21
	v_mul_f32_e32 v6, v5, v6
	v_mul_f32_e32 v7, v5, v7
	global_store_dword v10, v15, s[60:61] offset:16
	v_mul_f32_e32 v13, v5, v22
	v_mul_f32_e32 v14, v5, v23
	v_med3_f32 v11, v11, s35, v225
	v_med3_f32 v12, v12, s35, v225
	v_mov_b32_e32 v15, v4
	v_mul_f32_e32 v8, v5, v8
	v_mul_f32_e32 v5, v5, v9
	v_med3_f32 v6, v6, s35, v225
	v_med3_f32 v7, v7, s35, v225
	v_mov_b32_e32 v9, v4
	v_cvt_pk_fp8_f32 v15, v11, v12
	v_cvt_pk_fp8_f32 v9, v6, v7
	v_med3_f32 v11, v13, s35, v225
	v_med3_f32 v12, v14, s35, v225
	v_med3_f32 v6, v8, s35, v225
	v_med3_f32 v5, v5, s35, v225
	v_cvt_pk_fp8_f32 v15, v11, v12 op_sel:[0,0,1]
	v_cvt_pk_fp8_f32 v9, v6, v5 op_sel:[0,0,1]
	global_store_dword v10, v15, s[60:61] offset:32
	global_store_dword v10, v9, s[60:61] offset:48
	s_and_saveexec_b64 s[44:45], s[42:43]
	s_cbranch_execz .LBB0_697
	v_log_f32_e32 v2, v2
	v_lshl_or_b32 v3, v3, 5, s80
	v_add_f32_e32 v2, v84, v2
	global_store_dword v3, v2, s[30:31]

; #define GAS __attribute__((address_space(1)))
; #define LAS __attribute__((address_space(3)))
; DI int rfl(int v) { return __builtin_amdgcn_readfirstlane(v); }
; DI int ltid() { int t = threadIdx.x; asm volatile("" : "+v"(t)); return t; }
; #define AT_BAR() do { asm volatile("s_waitcnt lgkmcnt(0)" ::: "memory"); __builtin_amdgcn_s_barrier(); asm volatile("" ::: "memory"); } while (0)
; DI void attn_load(const Ctx& c, int u, APre& p) {
;     const int tid = ltid(), lane = tid & 63, w = rfl(tid >> 6), fr = lane & 15, fq = lane >> 4; const AUnit a = attn_decode(u);
;     const GAS char* Q = (const GAS char*)(c.ws + WS_H + H_QD) + a.slab; const GAS char* K = (const GAS char*)(c.ws + WS_H + H_KD) + a.slab; const GAS char* V = (const GAS char*)(c.ws + WS_H + H_VD) + a.slab;
; #pragma unroll
;     for (int b = 0; b < 2; ++b) { const unsigned jq = (unsigned)(128 * (a.n + b) + 16 * w + fr);
; #pragma unroll
;         for (int d0 = 0; d0 < 2; ++d0) p.q[b][d0] = *(const GAS u32x2*)(Q + (jq * 64u + (unsigned)(32 * d0 + 8 * fq))); }
; #pragma unroll
;     for (int c2 = 0; c2 < 6; ++c2) { const int idx = tid + NTHREADS * c2, row = idx >> 3, ch = idx & 7; const int j = 128 * (a.n - 1) + row;
;         p.k[c2] = (u32x2){0u, 0u}; p.v[c2] = (u32x2){0u, 0u};
;         if (j >= 0) { const unsigned off = (unsigned)j * 64u + (unsigned)(ch * 8); p.k[c2] = *(const GAS u32x2*)(K + off); p.v[c2] = *(const GAS u32x2*)(V + off); } }
; }
; DI void attn_stage(LAS unsigned char* lds, const APre& p) {
;     const int tid = ltid(); LAS bf16_t* Ks = (LAS bf16_t*)(lds + AT_K); LAS bf16_t* Vs = (LAS bf16_t*)(lds + AT_V);
; #pragma unroll
;     for (int c2 = 0; c2 < 6; ++c2) { const int o = (tid >> 3) * 72 + (tid & 7) * 8 + c2 * (64 * 72); *(LAS u32x4*)(Ks + o) = fp8x8_to_bf16(p.k[c2]); *(LAS u32x4*)(Vs + o) = fp8x8_to_bf16(p.v[c2]); }
; }
; DI void attn_pull(LAS unsigned char* lds, const Ctx& c, unsigned* ctr, int base, int limit) {
;     ...
;     while (cur < limit) {
;         AT_BAR();
;         const int nxt2 = rfl(TK[2]);
;         attn_stage(lds, pre);
;         bf16x8 qf[2][2];
; #pragma unroll
;         for (int b = 0; b < 2; ++b)
; #pragma unroll
;             for (int d0 = 0; d0 < 2; ++d0) qf[b][d0] = __builtin_bit_cast(bf16x8, fp8x8_to_bf16(pre.q[b][d0]));
;         AT_BAR();
;         if (nxt < limit) attn_load(c, nxt, pre);
.LBB0_796:
	s_waitcnt lgkmcnt(0)
	s_barrier
	v_mov_b32_e32 v1, s78
	v_mov_b32_e32 v5, v0
	ds_read_b32 v1, v1
	s_movk_i32 s7, 0x50
	v_lshrrev_b32_e32 v9, 3, v5
	v_lshlrev_b32_e32 v5, 3, v5
	v_and_b32_e32 v8, 56, v5
	v_mad_u64_u32 v[12:13], s[8:9], v9, s7, v[8:9]
	v_cvt_pk_f32_fp8_e32 v[8:9], v44
	v_cvt_pk_f32_fp8_sdwa v[10:11], v44 src0_sel:WORD_1
	v_cvt_pk_f32_fp8_e32 v[14:15], v45
	v_cvt_pk_f32_fp8_sdwa v[16:17], v45 src0_sel:WORD_1
	v_cvt_pk_bf16_f32 v8, v8, v9
	v_cvt_pk_bf16_f32 v9, v10, v11
	v_cvt_pk_bf16_f32 v10, v14, v15
	v_cvt_pk_bf16_f32 v11, v16, v17
	v_lshl_add_u32 v5, v12, 1, s38
	v_add_u32_e32 v196, 0xf000, v5
	ds_write_b128 v5, v[8:11]
	v_cvt_pk_f32_fp8_e32 v[8:9], v46
	v_cvt_pk_f32_fp8_sdwa v[10:11], v46 src0_sel:WORD_1
	v_cvt_pk_f32_fp8_e32 v[12:13], v47
	v_cvt_pk_f32_fp8_sdwa v[14:15], v47 src0_sel:WORD_1
	v_cvt_pk_bf16_f32 v8, v8, v9
	v_cvt_pk_bf16_f32 v9, v10, v11
	v_cvt_pk_bf16_f32 v10, v12, v13
	v_cvt_pk_bf16_f32 v11, v14, v15
	ds_write_b128 v196, v[8:11]
	v_cvt_pk_f32_fp8_e32 v[8:9], v48
	v_cvt_pk_f32_fp8_sdwa v[10:11], v48 src0_sel:WORD_1
	v_cvt_pk_f32_fp8_e32 v[12:13], v49
	v_cvt_pk_f32_fp8_sdwa v[14:15], v49 src0_sel:WORD_1
	v_cvt_pk_bf16_f32 v8, v8, v9
	v_cvt_pk_bf16_f32 v9, v10, v11
	v_cvt_pk_bf16_f32 v10, v12, v13
	v_cvt_pk_bf16_f32 v11, v14, v15
	ds_write_b128 v5, v[8:11] offset:10240
	v_cvt_pk_f32_fp8_e32 v[8:9], v42
	v_cvt_pk_f32_fp8_sdwa v[10:11], v42 src0_sel:WORD_1
	v_cvt_pk_f32_fp8_e32 v[12:13], v43
	v_cvt_pk_f32_fp8_sdwa v[14:15], v43 src0_sel:WORD_1
	v_cvt_pk_bf16_f32 v8, v8, v9
	v_cvt_pk_bf16_f32 v9, v10, v11
	v_cvt_pk_bf16_f32 v10, v12, v13
	v_cvt_pk_bf16_f32 v11, v14, v15
	ds_write_b128 v196, v[8:11] offset:10240
	v_cvt_pk_f32_fp8_e32 v[8:9], v50
	v_cvt_pk_f32_fp8_sdwa v[10:11], v50 src0_sel:WORD_1
	v_cvt_pk_f32_fp8_e32 v[12:13], v51
	v_cvt_pk_f32_fp8_sdwa v[14:15], v51 src0_sel:WORD_1
	v_cvt_pk_bf16_f32 v8, v8, v9
	v_cvt_pk_bf16_f32 v9, v10, v11
	v_cvt_pk_bf16_f32 v10, v12, v13
	v_cvt_pk_bf16_f32 v11, v14, v15
	ds_write_b128 v5, v[8:11] offset:20480
	v_cvt_pk_f32_fp8_e32 v[8:9], v52
	v_cvt_pk_f32_fp8_sdwa v[10:11], v52 src0_sel:WORD_1
	v_cvt_pk_f32_fp8_e32 v[12:13], v53
	v_cvt_pk_f32_fp8_sdwa v[14:15], v53 src0_sel:WORD_1
	v_add_u32_e32 v16, 0xd800, v5
	v_cvt_pk_bf16_f32 v8, v8, v9
	v_cvt_pk_bf16_f32 v9, v10, v11
	v_cvt_pk_bf16_f32 v10, v12, v13
	v_cvt_pk_bf16_f32 v11, v14, v15
	ds_write_b128 v196, v[8:11] offset:20480
	v_cvt_pk_f32_fp8_e32 v[8:9], v62
	v_cvt_pk_f32_fp8_sdwa v[10:11], v62 src0_sel:WORD_1
	v_cvt_pk_f32_fp8_e32 v[12:13], v63
	v_cvt_pk_f32_fp8_sdwa v[14:15], v63 src0_sel:WORD_1
	v_cvt_pk_bf16_f32 v8, v8, v9
	v_cvt_pk_bf16_f32 v9, v10, v11
	v_cvt_pk_bf16_f32 v10, v12, v13
	v_cvt_pk_bf16_f32 v11, v14, v15
	ds_write_b128 v5, v[8:11] offset:30720
	v_cvt_pk_f32_fp8_e32 v[8:9], v64
	v_cvt_pk_f32_fp8_sdwa v[10:11], v64 src0_sel:WORD_1
	v_cvt_pk_f32_fp8_e32 v[12:13], v65
	v_cvt_pk_f32_fp8_sdwa v[14:15], v65 src0_sel:WORD_1
	v_cvt_pk_bf16_f32 v8, v8, v9
	v_cvt_pk_bf16_f32 v9, v10, v11
	v_cvt_pk_bf16_f32 v10, v12, v13
	v_cvt_pk_bf16_f32 v11, v14, v15
	ds_write_b128 v196, v[8:11] offset:30720
	v_cvt_pk_f32_fp8_e32 v[8:9], v66
	v_cvt_pk_f32_fp8_sdwa v[10:11], v66 src0_sel:WORD_1
	v_cvt_pk_f32_fp8_e32 v[12:13], v67
	v_cvt_pk_f32_fp8_sdwa v[14:15], v67 src0_sel:WORD_1
	v_cvt_pk_bf16_f32 v8, v8, v9
	v_cvt_pk_bf16_f32 v9, v10, v11
	v_cvt_pk_bf16_f32 v10, v12, v13
	v_cvt_pk_bf16_f32 v11, v14, v15
	ds_write_b128 v5, v[8:11] offset:40960
	v_cvt_pk_f32_fp8_e32 v[8:9], v68
	v_cvt_pk_f32_fp8_sdwa v[10:11], v68 src0_sel:WORD_1
	v_cvt_pk_f32_fp8_e32 v[12:13], v69
	v_cvt_pk_f32_fp8_sdwa v[14:15], v69 src0_sel:WORD_1
	v_cvt_pk_bf16_f32 v8, v8, v9
	v_cvt_pk_bf16_f32 v9, v10, v11
	v_cvt_pk_bf16_f32 v10, v12, v13
	v_cvt_pk_bf16_f32 v11, v14, v15
	ds_write_b128 v196, v[8:11] offset:40960
	v_cvt_pk_f32_fp8_e32 v[8:9], v70
	v_cvt_pk_f32_fp8_sdwa v[10:11], v70 src0_sel:WORD_1
	v_cvt_pk_f32_fp8_e32 v[12:13], v71
	v_cvt_pk_f32_fp8_sdwa v[14:15], v71 src0_sel:WORD_1
	v_cvt_pk_bf16_f32 v8, v8, v9
	v_cvt_pk_bf16_f32 v9, v10, v11
	v_cvt_pk_bf16_f32 v10, v12, v13
	v_cvt_pk_bf16_f32 v11, v14, v15
	ds_write_b128 v5, v[8:11] offset:51200
	v_cvt_pk_f32_fp8_e32 v[8:9], v72
	v_cvt_pk_f32_fp8_sdwa v[10:11], v72 src0_sel:WORD_1
	v_cvt_pk_f32_fp8_e32 v[12:13], v73
	v_cvt_pk_f32_fp8_sdwa v[14:15], v73 src0_sel:WORD_1
	v_cvt_pk_bf16_f32 v8, v8, v9
	v_cvt_pk_bf16_f32 v9, v10, v11
	v_cvt_pk_bf16_f32 v10, v12, v13
	v_cvt_pk_bf16_f32 v11, v14, v15
	ds_write_b128 v196, v[8:11] offset:51200
	s_waitcnt lgkmcnt(0)
	s_barrier
	s_cmpk_gt_i32 s4, 0x17ff
	s_cselect_b64 s[62:63], -1, 0
	s_waitcnt lgkmcnt(12)
	v_readfirstlane_b32 s79, v1
	s_and_b64 vcc, exec, s[62:63]
	s_cbranch_vccnz .LBB0_810
	s_ashr_i32 s8, s4, 31
	s_lshr_b32 s8, s8, 24
	s_add_i32 s8, s4, s8
	s_ashr_i32 s8, s8, 8
	s_mul_hi_i32 s9, s8, 0x55555556
	s_lshr_b32 s10, s9, 31
	s_add_i32 s9, s9, s10
	s_mul_hi_i32 s10, s4, 0x2aaaaaab
	s_mul_i32 s9, s9, 3
	s_lshr_b32 s11, s10, 31
	s_lshr_b32 s10, s10, 7
	s_sub_i32 s8, s8, s9
	s_and_b32 s9, s4, 31
	s_add_i32 s10, s10, s11
	s_cmp_eq_u32 s8, 1
	s_cselect_b32 s11, 2, 4
	s_cmp_lg_u32 s8, 0
	s_cselect_b32 s11, s11, 0
	s_sub_i32 s43, 5, s11
	s_lshr_b32 s42, 32, s11
	s_lshr_b32 s43, s9, s43
	s_mul_i32 s42, s43, s42
	s_sub_i32 s46, s9, s42
	s_sub_i32 s9, 12, s11
	s_lshl_b32 s11, s4, 16
	s_and_b32 s11, s11, 0xe00000
	s_lshl_b32 s10, s10, 18
	s_lshl_b32 s9, s43, s9
	s_lshl_b32 s8, s8, 24
	s_add_i32 s10, s11, s10
	s_add_i32 s8, s10, s8
	s_lshl_b32 s9, s9, 6
	v_mov_b32_e32 v1, v0
	s_add_i32 s10, s8, s9
	s_add_u32 s8, s5, s10
	v_readfirstlane_b32 s7, v1
	s_addc_u32 s9, s39, 0
	s_lshr_b32 s7, s7, 2
	s_and_b32 s7, s7, 0x3fffff0
	v_and_or_b32 v5, v1, 15, s7
	s_lshl_b32 s7, s46, 13
	v_lshrrev_b32_e32 v8, 1, v1
	v_lshl_add_u32 v5, v5, 6, s7
	v_and_or_b32 v5, v8, 24, v5
	v_add_u32_e32 v8, 0x2000, v5
	global_load_dwordx2 v[60:61], v5, s[8:9]
	global_load_dwordx2 v[58:59], v5, s[8:9] offset:32
	global_load_dwordx2 v[56:57], v8, s[8:9]
	global_load_dwordx2 v[54:55], v8, s[8:9] offset:32
	s_add_u32 s42, s68, s10
	s_addc_u32 s43, s74, 0
	s_add_u32 s44, s75, s10
	s_addc_u32 s45, s76, 0
	s_lshl_b32 s7, s46, 7
	v_lshlrev_b32_e32 v5, 3, v1
	s_addk_i32 s7, 0xff80
	v_and_b32_e32 v8, 56, v5
	v_ashrrev_i32_e32 v5, 3, v1
	v_add_u32_e32 v5, s7, v5
	v_mov_b32_e32 v42, v4
	v_mov_b32_e32 v43, v4
	v_cmp_lt_i32_e32 vcc, -1, v5
	v_mov_b64_e32 v[46:47], v[42:43]
	v_mov_b64_e32 v[44:45], v[42:43]
	s_and_saveexec_b64 s[46:47], vcc
	s_cbranch_execz .LBB0_799
	v_lshl_or_b32 v5, v5, 6, v8
	global_load_dwordx2 v[44:45], v5, s[42:43]
	global_load_dwordx2 v[46:47], v5, s[44:45]
